# speedup vs baseline: 1.0168x; 1.0061x over previous
_Z11gemm_kernelILi1EEvPKDF16_S1_PKfPDF16_PfS5_S3_S3_S1_S3_:
	s_cmpk_lt_u32 s2, 0x1b
	s_cbranch_scc0 .Lprio_g1
	s_setprio 3
.Lprio_g1:
	v_lshrrev_b32_e32 v4, 5, v0
	s_lshl_b32 s17, s2, 5
	v_or_b32_e32 v1, s17, v4
	s_load_dwordx4 s[8:11], s[0:1], 0x0
	s_load_dwordx2 s[12:13], s[0:1], 0x28
	v_or_b32_e32 v2, 8, v1
	v_min_i32_e32 v6, 0xc34f, v1
	v_min_i32_e32 v10, 0xc34f, v2
	v_ashrrev_i32_e32 v7, 31, v6
	v_ashrrev_i32_e32 v11, 31, v10
	v_mov_b32_e32 v3, 0
	v_and_b32_e32 v5, 31, v0
	v_lshlrev_b64 v[6:7], 9, v[6:7]
	v_lshlrev_b64 v[10:11], 9, v[10:11]
	s_waitcnt lgkmcnt(0)
	v_lshl_add_u64 v[6:7], s[8:9], 0, v[6:7]
	v_lshlrev_b32_e32 v8, 4, v5
	v_mov_b32_e32 v9, v3
	v_lshl_add_u64 v[10:11], s[8:9], 0, v[10:11]
	v_lshl_add_u64 v[6:7], v[6:7], 0, v[8:9]
	v_lshl_add_u64 v[10:11], v[10:11], 0, v[8:9]
	v_or_b32_e32 v2, 16, v1
	v_or_b32_e32 v1, 24, v1
	global_load_dwordx4 v[34:37], v[6:7], off nt
	global_load_dwordx4 v[38:41], v[10:11], off nt
	v_min_i32_e32 v6, 0xc34f, v2
	v_min_i32_e32 v10, 0xc34f, v1
	v_ashrrev_i32_e32 v7, 31, v6
	v_ashrrev_i32_e32 v11, 31, v10
	v_lshlrev_b64 v[6:7], 9, v[6:7]
	v_lshlrev_b64 v[10:11], 9, v[10:11]
	v_lshl_add_u64 v[6:7], s[8:9], 0, v[6:7]
	v_lshl_add_u64 v[10:11], s[8:9], 0, v[10:11]
	v_lshlrev_b32_e32 v2, 9, v0
	v_lshl_add_u64 v[6:7], v[6:7], 0, v[8:9]
	v_lshl_add_u64 v[10:11], v[10:11], 0, v[8:9]
	v_and_b32_e32 v1, 63, v0
	v_and_b32_e32 v9, 0x18000, v2
	v_lshl_or_b32 v2, v1, 4, v9
	v_lshlrev_b32_e32 v1, 4, v0
	s_movk_i32 s3, 0x7c00
	global_load_dwordx4 v[58:61], v[6:7], off nt
	global_load_dwordx4 v[70:73], v[10:11], off nt
	v_lshl_add_u64 v[6:7], s[10:11], 0, v[2:3]
	v_or3_b32 v1, v1, v9, s3
	s_movk_i32 s3, 0x1000
	v_add_co_u32_e32 v10, vcc, s3, v6
	s_movk_i32 s3, 0x2000
	s_nop 0
	v_addc_co_u32_e32 v11, vcc, 0, v7, vcc
	v_add_co_u32_e32 v12, vcc, s3, v6
	s_movk_i32 s4, 0x3000
	s_nop 0
	v_addc_co_u32_e32 v13, vcc, 0, v7, vcc
	v_add_co_u32_e32 v14, vcc, s4, v6
	s_movk_i32 s4, 0x4000
	s_nop 0
	v_addc_co_u32_e32 v15, vcc, 0, v7, vcc
	v_add_co_u32_e32 v16, vcc, s4, v6
	s_movk_i32 s4, 0x5000
	s_nop 0
	v_addc_co_u32_e32 v17, vcc, 0, v7, vcc
	global_load_dwordx4 v[42:45], v[10:11], off offset:1024
	global_load_dwordx4 v[46:49], v[10:11], off offset:2048
	global_load_dwordx4 v[50:53], v[12:13], off offset:-4096
	global_load_dwordx4 v[54:57], v[12:13], off
	global_load_dwordx4 v[62:65], v[12:13], off offset:1024
	global_load_dwordx4 v[66:69], v[12:13], off offset:2048
	global_load_dwordx4 v[74:77], v[12:13], off offset:3072
	global_load_dwordx4 v[78:81], v[16:17], off offset:-4096
	global_load_dwordx4 v[82:85], v[10:11], off offset:3072
	global_load_dwordx4 v[86:89], v[14:15], off offset:1024
	global_load_dwordx4 v[90:93], v[14:15], off offset:2048
	global_load_dwordx4 v[94:97], v[14:15], off offset:3072
	global_load_dwordx4 v[98:101], v[16:17], off
	global_load_dwordx4 v[102:105], v[16:17], off offset:1024
	global_load_dwordx4 v[106:109], v2, s[10:11]
	global_load_dwordx4 v[110:113], v2, s[10:11] offset:1024
	global_load_dwordx4 v[114:117], v2, s[10:11] offset:2048
	global_load_dwordx4 v[118:121], v2, s[10:11] offset:3072
	global_load_dwordx4 v[122:125], v[16:17], off offset:2048
	global_load_dwordx4 v[126:129], v[16:17], off offset:3072
	v_add_co_u32_e32 v10, vcc, s4, v6
	s_movk_i32 s4, 0x6000
	s_nop 0
	v_addc_co_u32_e32 v11, vcc, 0, v7, vcc
	v_add_co_u32_e32 v12, vcc, s4, v6
	s_movk_i32 s4, 0x7000
	s_nop 0
	v_addc_co_u32_e32 v13, vcc, 0, v7, vcc
	v_add_co_u32_e32 v6, vcc, s4, v6
	global_load_dwordx4 v[130:133], v[12:13], off offset:-4096
	global_load_dwordx4 v[134:137], v[12:13], off
	global_load_dwordx4 v[138:141], v[10:11], off offset:1024
	global_load_dwordx4 v[142:145], v[10:11], off offset:2048
	global_load_dwordx4 v[146:149], v[10:11], off offset:3072
	v_addc_co_u32_e32 v7, vcc, 0, v7, vcc
	global_load_dwordx4 v[150:153], v[12:13], off offset:1024
	global_load_dwordx4 v[154:157], v[12:13], off offset:2048
	global_load_dwordx4 v[158:161], v[12:13], off offset:3072
	global_load_dwordx4 v[162:165], v[6:7], off
	global_load_dwordx4 v[166:169], v[6:7], off offset:1024
	global_load_dwordx4 v[170:173], v[6:7], off offset:2048
	global_load_dwordx4 v[174:177], v1, s[10:11]
	s_movk_i32 s10, 0x210
	v_mad_u32_u24 v213, v4, s10, v8
	s_mov_b32 s14, 0
	s_cmpk_gt_i32 s2, 0x61a
	v_bfe_u32 v1, v0, 4, 2
	v_and_b32_e32 v212, 15, v0
	s_waitcnt vmcnt(35)
	ds_write_b128 v213, v[34:37]
	s_waitcnt vmcnt(34)
	ds_write_b128 v213, v[38:41] offset:4224
	s_waitcnt vmcnt(33)
	ds_write_b128 v213, v[58:61] offset:8448
	s_waitcnt vmcnt(32)
	ds_write_b128 v213, v[70:73] offset:12672
	s_waitcnt vmcnt(17)
	s_waitcnt vmcnt(16)
	s_waitcnt vmcnt(15)
	s_waitcnt vmcnt(14)
	s_waitcnt vmcnt(13)
	s_waitcnt vmcnt(12)
	s_waitcnt vmcnt(11)
	s_waitcnt vmcnt(9)
	s_waitcnt vmcnt(8)
	s_waitcnt vmcnt(7)
	s_waitcnt vmcnt(6)
	s_waitcnt vmcnt(5)
	s_waitcnt vmcnt(4)
	s_waitcnt vmcnt(3)
	s_waitcnt vmcnt(2)
	s_waitcnt vmcnt(1)
	s_waitcnt vmcnt(0)
	s_waitcnt lgkmcnt(0)
	s_barrier
	s_cbranch_scc1 .LBB2_11
	s_load_dwordx2 s[4:5], s[0:1], 0x18
	s_load_dword s15, s[0:1], 0x50
	v_lshlrev_b32_e32 v2, 3, v5
	v_lshlrev_b32_e32 v2, 1, v2
	v_lshl_add_u64 v[210:211], s[8:9], 0, v[2:3]
	v_and_b32_e32 v2, 48, v0
	s_waitcnt lgkmcnt(0)
	s_add_i32 s0, s2, s15
	v_lshl_or_b32 v215, s0, 5, v4
	v_lshlrev_b32_e32 v4, 1, v0
	v_mad_u32_u24 v214, v212, s10, v2
	s_lshl_b32 s0, s2, 14
	v_lshlrev_b32_e32 v2, 9, v212
	v_and_b32_e32 v4, 0x180, v4
	v_mov_b32_e32 v16, v3
	v_mov_b32_e32 v17, v3
	v_or3_b32 v218, s0, v2, v4
	v_mov_b32_e32 v2, v3
	v_mov_b32_e32 v4, v3
	v_mov_b32_e32 v5, v3
	v_mov_b32_e32 v6, v3
	v_mov_b32_e32 v7, v3
	v_mov_b32_e32 v8, v3
	v_mov_b32_e32 v9, v3
	v_mov_b32_e32 v10, v3
	v_mov_b32_e32 v11, v3
	v_mov_b32_e32 v12, v3
	v_mov_b32_e32 v13, v3
	v_mov_b32_e32 v14, v3
	v_mov_b32_e32 v15, v3
	v_mov_b64_e32 v[32:33], v[16:17]
	s_mov_b32 s7, 0x20000
	s_mov_b32 s6, 0x186a000
	s_and_b32 s5, s5, 0xffff
	s_lshl_b32 s16, s15, 5
	v_add_u32_e32 v216, s17, v212
	v_lshlrev_b32_e32 v217, 4, v1
	s_lshl_b32 s17, s15, 14
	s_mov_b32 s18, 0xc350
	s_mov_b32 s19, s2
	s_mov_b32 s20, 0
	v_mov_b64_e32 v[30:31], v[14:15]
	v_mov_b64_e32 v[28:29], v[12:13]
	v_mov_b64_e32 v[26:27], v[10:11]
	v_mov_b64_e32 v[24:25], v[8:9]
	v_mov_b64_e32 v[22:23], v[6:7]
	v_mov_b64_e32 v[20:21], v[4:5]
	v_mov_b64_e32 v[18:19], v[2:3]
	s_branch .LBB2_3

_Z11gemm_kernelILi2EEvPKDF16_S1_PKfPDF16_PfS5_S3_S3_S1_S3_:
	s_cmpk_lt_u32 s2, 0x1b
	s_cbranch_scc0 .Lprio_g2
	s_setprio 3
.Lprio_g2:
	s_load_dwordx4 s[8:11], s[0:1], 0x28
	s_load_dwordx4 s[4:7], s[0:1], 0x0
	v_mov_b32_e32 v211, 0
	v_lshlrev_b32_e32 v178, 2, v0
	v_mov_b32_e32 v179, v211
	s_waitcnt lgkmcnt(0)
	v_lshl_add_u64 v[2:3], s[8:9], 0, v[178:179]
	s_movk_i32 s3, 0x1000
	v_add_co_u32_e32 v4, vcc, s3, v2
	s_movk_i32 s14, 0x2000
	s_nop 0
	v_addc_co_u32_e32 v5, vcc, 0, v3, vcc
	v_add_co_u32_e32 v6, vcc, s14, v2
	s_movk_i32 s15, 0x3000
	s_nop 0
	v_addc_co_u32_e32 v7, vcc, 0, v3, vcc
	global_load_dword v46, v[6:7], off
	global_load_dword v47, v[6:7], off offset:1024
	global_load_dword v48, v[6:7], off offset:2048
	global_load_dword v49, v[6:7], off offset:3072
	v_add_co_u32_e32 v2, vcc, s15, v2
	v_lshrrev_b32_e32 v1, 6, v0
	s_nop 0
	v_addc_co_u32_e32 v3, vcc, 0, v3, vcc
	global_load_dword v50, v[2:3], off
	global_load_dword v51, v[2:3], off offset:1024
	global_load_dword v52, v[2:3], off offset:2048
	global_load_dword v53, v[2:3], off offset:3072
	s_load_dwordx2 s[8:9], s[0:1], 0x48
	s_load_dwordx2 s[12:13], s[0:1], 0x38
	global_load_dword v54, v178, s[10:11]
	s_waitcnt lgkmcnt(0)
	global_load_dword v112, v178, s[8:9]
	global_load_dword v120, v178, s[12:13]
	v_lshlrev_b32_e32 v2, 4, v0
	v_and_b32_e32 v2, 0x3f0, v2
	v_lshl_or_b32 v210, v1, 15, v2
	v_lshl_add_u64 v[94:95], s[6:7], 0, v[210:211]
	v_add_co_u32_e32 v42, vcc, s3, v94
	s_movk_i32 s9, 0x4000
	s_nop 0
	v_addc_co_u32_e32 v43, vcc, 0, v95, vcc
	v_add_co_u32_e32 v34, vcc, s14, v94
	s_mov_b32 s8, 0x800000
	s_nop 0
	v_addc_co_u32_e32 v35, vcc, 0, v95, vcc
	v_add_co_u32_e32 v66, vcc, s15, v94
	s_movk_i32 s3, 0x5000
	s_nop 0
	v_addc_co_u32_e32 v67, vcc, 0, v95, vcc
	v_add_co_u32_e32 v68, vcc, s9, v94
	v_lshrrev_b32_e32 v180, 5, v0
	s_nop 0
	v_addc_co_u32_e32 v69, vcc, 0, v95, vcc
	global_load_dwordx4 v[2:5], v[42:43], off offset:1024
	global_load_dwordx4 v[6:9], v[42:43], off offset:2048
	global_load_dwordx4 v[10:13], v[34:35], off offset:-4096
	global_load_dwordx4 v[14:17], v[34:35], off
	global_load_dwordx4 v[18:21], v[34:35], off offset:1024
	global_load_dwordx4 v[22:25], v[34:35], off offset:2048
	global_load_dwordx4 v[26:29], v[34:35], off offset:3072
	global_load_dwordx4 v[30:33], v[68:69], off offset:-4096
	v_and_b32_e32 v179, 31, v0
	v_lshlrev_b32_e32 v142, 5, v179
	s_waitcnt vmcnt(18)
	v_add_f32_e32 v34, 0, v46
	s_waitcnt vmcnt(17)
	v_add_f32_e32 v35, 0, v47
	s_waitcnt vmcnt(16)
	v_add_f32_e32 v34, v34, v48
	s_waitcnt vmcnt(15)
	v_add_f32_e32 v35, v35, v49
	s_waitcnt vmcnt(14)
	v_add_f32_e32 v34, v34, v50
	s_waitcnt vmcnt(13)
	v_add_f32_e32 v35, v35, v51
	s_waitcnt vmcnt(12)
	v_add_f32_e32 v44, v34, v52
	s_waitcnt vmcnt(11)
	v_add_f32_e32 v34, v35, v53
	v_mul_f32_e32 v35, 0x37a7c5ac, v44
	v_mul_f32_e32 v34, 0x37a7c5ac, v34
	v_fma_f32 v34, -v35, v35, v34
	v_add_f32_e32 v34, 0x3727c5ac, v34
	v_mul_f32_e32 v35, 0x4b800000, v34
	v_cmp_gt_f32_e32 vcc, s8, v34
	s_waitcnt vmcnt(9)
	v_fmamk_f32 v113, v44, 0x37a7c5ac, v112
	v_cndmask_b32_e32 v34, v34, v35, vcc
	v_rsq_f32_e32 v45, v34
	global_load_dwordx4 v[34:37], v[42:43], off offset:3072
	global_load_dwordx4 v[38:41], v[66:67], off offset:1024
	v_mul_f32_e32 v42, 0x45800000, v45
	v_cndmask_b32_e32 v42, v45, v42, vcc
	v_add_co_u32_e32 v110, vcc, s3, v94
	s_movk_i32 s3, 0x6000
	s_nop 0
	v_addc_co_u32_e32 v111, vcc, 0, v95, vcc
	v_add_co_u32_e32 v96, vcc, s3, v94
	s_movk_i32 s3, 0x7000
	s_nop 0
	v_addc_co_u32_e32 v97, vcc, 0, v95, vcc
	v_add_co_u32_e32 v118, vcc, s3, v94
	v_mul_f32_e32 v121, v42, v54
	global_load_dwordx4 v[42:45], v[66:67], off offset:2048
	global_load_dwordx4 v[46:49], v[66:67], off offset:3072
	global_load_dwordx4 v[50:53], v[68:69], off
	global_load_dwordx4 v[54:57], v[68:69], off offset:1024
	global_load_dwordx4 v[58:61], v[68:69], off offset:2048
	global_load_dwordx4 v[62:65], v[68:69], off offset:3072
	s_nop 0
	global_load_dwordx4 v[66:69], v[110:111], off offset:1024
	global_load_dwordx4 v[70:73], v[110:111], off offset:2048
	global_load_dwordx4 v[74:77], v[96:97], off offset:-4096
	global_load_dwordx4 v[78:81], v[96:97], off
	global_load_dwordx4 v[82:85], v[96:97], off offset:1024
	global_load_dwordx4 v[86:89], v[96:97], off offset:2048
	global_load_dwordx4 v[90:93], v[96:97], off offset:3072
	v_addc_co_u32_e32 v119, vcc, 0, v95, vcc
	global_load_dwordx4 v[94:97], v[110:111], off offset:3072
	global_load_dwordx4 v[98:101], v[118:119], off
	global_load_dwordx4 v[102:105], v[118:119], off offset:1024
	global_load_dwordx4 v[106:109], v[118:119], off offset:2048
	v_sub_f32_e32 v110, v112, v113
	s_waitcnt vmcnt(27)
	v_fmac_f32_e32 v120, v110, v121
	global_load_dwordx4 v[110:113], v210, s[6:7]
	global_load_dwordx4 v[114:117], v[118:119], off offset:3072
	ds_write2st64_b32 v178, v121, v120 offset1:4
	global_load_dwordx4 v[118:121], v210, s[6:7] offset:1024
	global_load_dwordx4 v[122:125], v210, s[6:7] offset:2048
	global_load_dwordx4 v[126:129], v210, s[6:7] offset:3072
	s_lshl_b32 s6, s2, 5
	v_or_b32_e32 v158, s6, v180
	v_min_i32_e32 v146, 0xc34f, v158
	v_ashrrev_i32_e32 v147, 31, v146
	v_lshlrev_b64 v[146:147], 9, v[146:147]
	v_lshl_add_u64 v[146:147], s[4:5], 0, v[146:147]
	v_lshlrev_b32_e32 v210, 4, v179
	v_lshl_add_u64 v[146:147], v[146:147], 0, v[210:211]
	s_waitcnt lgkmcnt(0)
	s_barrier
	ds_read_b128 v[130:133], v142
	ds_read_b128 v[134:137], v142 offset:16
	ds_read_b128 v[138:141], v142 offset:1024
	ds_read_b128 v[142:145], v142 offset:1040
	s_waitcnt lgkmcnt(0)
	s_barrier
	global_load_dwordx4 v[146:149], v[146:147], off nt
	v_or_b32_e32 v150, 8, v158
	v_min_i32_e32 v150, 0xc34f, v150
	v_ashrrev_i32_e32 v151, 31, v150
	v_lshlrev_b64 v[150:151], 9, v[150:151]
	v_lshl_add_u64 v[150:151], s[4:5], 0, v[150:151]
	v_lshl_add_u64 v[150:151], v[150:151], 0, v[210:211]
	global_load_dwordx4 v[150:153], v[150:151], off nt
	v_or_b32_e32 v154, 16, v158
	v_min_i32_e32 v154, 0xc34f, v154
	v_ashrrev_i32_e32 v155, 31, v154
	v_lshlrev_b64 v[154:155], 9, v[154:155]
	v_lshl_add_u64 v[154:155], s[4:5], 0, v[154:155]
	v_lshl_add_u64 v[154:155], v[154:155], 0, v[210:211]
	global_load_dwordx4 v[154:157], v[154:155], off nt
	v_or_b32_e32 v158, 24, v158
	v_min_i32_e32 v158, 0xc34f, v158
	v_ashrrev_i32_e32 v159, 31, v158
	v_lshlrev_b64 v[158:159], 9, v[158:159]
	v_lshl_add_u64 v[158:159], s[4:5], 0, v[158:159]
	v_lshl_add_u64 v[158:159], v[158:159], 0, v[210:211]
	global_load_dwordx4 v[158:161], v[158:159], off nt
	s_movk_i32 s7, 0x210
	v_mad_u32_u24 v216, v180, s7, v210
	s_mov_b32 s3, 0
	s_cmpk_gt_i32 s2, 0x61a
	s_waitcnt vmcnt(3)
	v_cvt_f32_f16_e32 v162, v146
	v_cvt_f32_f16_sdwa v163, v146 dst_sel:DWORD dst_unused:UNUSED_PAD src0_sel:WORD_1
	v_cvt_f32_f16_e32 v164, v147
	v_cvt_f32_f16_sdwa v165, v147 dst_sel:DWORD dst_unused:UNUSED_PAD src0_sel:WORD_1
	v_pk_fma_f32 v[162:163], v[130:131], v[162:163], v[138:139]
	s_nop 0
	v_max_f32_e32 v166, 0, v163
	v_max_f32_e32 v167, 0, v162
	v_pk_fma_f32 v[162:163], v[132:133], v[164:165], v[140:141]
	v_cvt_f32_f16_e32 v164, v148
	v_cvt_f32_f16_sdwa v165, v148 dst_sel:DWORD dst_unused:UNUSED_PAD src0_sel:WORD_1
	v_max_f32_e32 v168, 0, v162
	v_cvt_pk_f16_f32 v162, v167, v166
	v_cvt_f32_f16_e32 v166, v149
	v_cvt_f32_f16_sdwa v167, v149 dst_sel:DWORD dst_unused:UNUSED_PAD src0_sel:WORD_1
	v_pk_fma_f32 v[164:165], v[134:135], v[164:165], v[142:143]
	v_max_f32_e32 v163, 0, v163
	v_max_f32_e32 v165, 0, v165
	v_max_f32_e32 v164, 0, v164
	v_pk_fma_f32 v[166:167], v[136:137], v[166:167], v[144:145]
	v_cvt_pk_f16_f32 v164, v164, v165
	v_max_f32_e32 v165, 0, v167
	v_max_f32_e32 v166, 0, v166
	v_cvt_pk_f16_f32 v163, v168, v163
	v_cvt_pk_f16_f32 v165, v166, v165
	s_waitcnt vmcnt(2)
	v_cvt_f32_f16_e32 v166, v150
	v_cvt_f32_f16_sdwa v167, v150 dst_sel:DWORD dst_unused:UNUSED_PAD src0_sel:WORD_1
	ds_write_b128 v216, v[162:165]
	v_cvt_f32_f16_e32 v162, v151
	v_cvt_f32_f16_sdwa v163, v151 dst_sel:DWORD dst_unused:UNUSED_PAD src0_sel:WORD_1
	v_pk_fma_f32 v[164:165], v[130:131], v[166:167], v[138:139]
	v_pk_fma_f32 v[162:163], v[132:133], v[162:163], v[140:141]
	v_max_f32_e32 v166, 0, v165
	v_max_f32_e32 v167, 0, v164
	v_cvt_f32_f16_e32 v164, v152
	v_cvt_f32_f16_sdwa v165, v152 dst_sel:DWORD dst_unused:UNUSED_PAD src0_sel:WORD_1
	v_max_f32_e32 v168, 0, v162
	v_cvt_pk_f16_f32 v162, v167, v166
	v_cvt_f32_f16_e32 v166, v153
	v_cvt_f32_f16_sdwa v167, v153 dst_sel:DWORD dst_unused:UNUSED_PAD src0_sel:WORD_1
	v_pk_fma_f32 v[164:165], v[134:135], v[164:165], v[142:143]
	v_max_f32_e32 v163, 0, v163
	v_max_f32_e32 v165, 0, v165
	v_max_f32_e32 v164, 0, v164
	v_pk_fma_f32 v[166:167], v[136:137], v[166:167], v[144:145]
	v_cvt_pk_f16_f32 v164, v164, v165
	v_max_f32_e32 v165, 0, v167
	v_max_f32_e32 v166, 0, v166
	v_cvt_pk_f16_f32 v163, v168, v163
	v_cvt_pk_f16_f32 v165, v166, v165
	s_waitcnt vmcnt(1)
	v_cvt_f32_f16_e32 v166, v154
	v_cvt_f32_f16_sdwa v167, v154 dst_sel:DWORD dst_unused:UNUSED_PAD src0_sel:WORD_1
	ds_write_b128 v216, v[162:165] offset:4224
	v_cvt_f32_f16_e32 v162, v155
	v_cvt_f32_f16_sdwa v163, v155 dst_sel:DWORD dst_unused:UNUSED_PAD src0_sel:WORD_1
	v_pk_fma_f32 v[164:165], v[130:131], v[166:167], v[138:139]
	v_pk_fma_f32 v[162:163], v[132:133], v[162:163], v[140:141]
	v_max_f32_e32 v166, 0, v165
	v_max_f32_e32 v167, 0, v164
	v_cvt_f32_f16_e32 v164, v156
	v_cvt_f32_f16_sdwa v165, v156 dst_sel:DWORD dst_unused:UNUSED_PAD src0_sel:WORD_1
	v_max_f32_e32 v168, 0, v162
	v_cvt_pk_f16_f32 v162, v167, v166
	v_cvt_f32_f16_e32 v166, v157
	v_cvt_f32_f16_sdwa v167, v157 dst_sel:DWORD dst_unused:UNUSED_PAD src0_sel:WORD_1
	v_pk_fma_f32 v[164:165], v[134:135], v[164:165], v[142:143]
	v_max_f32_e32 v163, 0, v163
	v_max_f32_e32 v165, 0, v165
	v_max_f32_e32 v164, 0, v164
	v_pk_fma_f32 v[166:167], v[136:137], v[166:167], v[144:145]
	v_cvt_pk_f16_f32 v164, v164, v165
	v_max_f32_e32 v165, 0, v167
	v_max_f32_e32 v166, 0, v166
	v_cvt_pk_f16_f32 v163, v168, v163
	v_cvt_pk_f16_f32 v165, v166, v165
	s_waitcnt vmcnt(0)
	v_cvt_f32_f16_e32 v166, v158
	v_cvt_f32_f16_sdwa v167, v158 dst_sel:DWORD dst_unused:UNUSED_PAD src0_sel:WORD_1
	ds_write_b128 v216, v[162:165] offset:8448
	v_cvt_f32_f16_e32 v162, v159
	v_cvt_f32_f16_sdwa v163, v159 dst_sel:DWORD dst_unused:UNUSED_PAD src0_sel:WORD_1
	v_pk_fma_f32 v[164:165], v[130:131], v[166:167], v[138:139]
	v_pk_fma_f32 v[162:163], v[132:133], v[162:163], v[140:141]
	v_max_f32_e32 v166, 0, v165
	v_max_f32_e32 v167, 0, v164
	v_cvt_f32_f16_e32 v164, v160
	v_cvt_f32_f16_sdwa v165, v160 dst_sel:DWORD dst_unused:UNUSED_PAD src0_sel:WORD_1
	v_max_f32_e32 v168, 0, v162
	v_cvt_pk_f16_f32 v162, v167, v166
	v_cvt_f32_f16_e32 v166, v161
	v_cvt_f32_f16_sdwa v167, v161 dst_sel:DWORD dst_unused:UNUSED_PAD src0_sel:WORD_1
	v_pk_fma_f32 v[164:165], v[134:135], v[164:165], v[142:143]
	v_max_f32_e32 v163, 0, v163
	v_max_f32_e32 v165, 0, v165
	v_max_f32_e32 v164, 0, v164
	v_pk_fma_f32 v[166:167], v[136:137], v[166:167], v[144:145]
	v_cvt_pk_f16_f32 v164, v164, v165
	v_max_f32_e32 v165, 0, v167
	v_max_f32_e32 v166, 0, v166
	v_cvt_pk_f16_f32 v163, v168, v163
	v_cvt_pk_f16_f32 v165, v166, v165
	ds_write_b128 v216, v[162:165] offset:12672
	s_waitcnt lgkmcnt(0)
	s_barrier
	s_cbranch_scc1 .LBB3_11
	v_lshrrev_b32_e32 v162, 2, v0
	s_load_dwordx2 s[10:11], s[0:1], 0x10
	s_load_dword s12, s[0:1], 0x50
	s_load_dwordx2 s[8:9], s[0:1], 0x20
	v_and_b32_e32 v181, 12, v162
	s_movk_i32 s13, 0xc0
	v_and_or_b32 v162, v0, s13, v181
	v_lshlrev_b32_e32 v174, 2, v162
	s_waitcnt lgkmcnt(0)
	global_load_dwordx4 v[162:165], v174, s[10:11]
	global_load_dwordx4 v[166:169], v174, s[10:11] offset:64
	global_load_dwordx4 v[170:173], v174, s[10:11] offset:128
	s_nop 0
	global_load_dwordx4 v[174:177], v174, s[10:11] offset:192
	s_load_dwordx2 s[0:1], s[0:1], 0x40
	v_lshlrev_b32_e32 v179, 3, v179
	v_lshlrev_b32_e32 v210, 1, v179
	v_and_b32_e32 v182, 15, v0
	v_lshl_add_u64 v[212:213], s[4:5], 0, v[210:211]
	v_and_b32_e32 v179, 48, v0
	v_mul_u32_u24_e32 v210, 0xc350, v1
	v_lshlrev_b32_e32 v0, 1, v181
	v_mov_b32_e32 v1, v211
	s_waitcnt lgkmcnt(0)
	v_lshl_add_u64 v[0:1], s[0:1], 0, v[0:1]
	s_add_i32 s0, s2, s12
	v_and_b32_e32 v178, 0x300, v178
	v_lshl_or_b32 v218, s0, 5, v180
	s_lshl_b32 s0, s2, 15
	v_lshlrev_b32_e32 v180, 10, v182
	v_or3_b32 v178, s0, v180, v178
	s_movk_i32 s0, 0x40c0
	s_mov_b32 s11, 0x20000
	s_mov_b32 s10, 0x30d4000
	s_and_b32 s9, s9, 0xffff
	s_mov_b32 s13, 0xc350
	v_mad_u32_u24 v217, v182, s7, v179
	s_lshl_b32 s14, s12, 5
	v_add_u32_e32 v219, s6, v182
	v_or3_b32 v220, v178, v179, s0
	s_lshl_b32 s15, s12, 15
	s_mov_b32 s16, 0
	s_branch .LBB3_3
